# re-measure: waves 4-7 barrier in front of the last two QK^T slices + sleep before softmax (same file)
# baseline (speedup 1.0000x reference)
.Lqkbar_m0_1:
	s_waitcnt lgkmcnt(2)
	v_mfma_f32_32x32x16_bf16 v[144:159], v[236:239], v[244:247], v[144:159]
	v_mfma_f32_32x32x16_bf16 v[128:143], v[240:243], v[244:247], v[128:143]
	s_waitcnt lgkmcnt(0)
	v_mfma_f32_32x32x16_bf16 v[144:159], v[248:251], v[166:169], v[144:159]
	v_mfma_f32_32x32x16_bf16 v[128:143], v[218:221], v[166:169], v[128:143]
	s_bitcmp0_b32 s100, 8
	s_cbranch_scc1 .Lstg_a10
	s_sleep 3
